# P1b: 16 serialized key-scale loads -> four 16-byte loads + one wait; diff-attention block entry waits leave the previous block's output stores in flight; put_next slots via ds_write
# baseline (speedup 1.0000x reference)
.LBB0_429:
	s_ashr_i32 s2, s7, 12
	v_lshl_or_b32 v4, s2, 2, v131
	v_ashrrev_i32_e32 v5, 31, v4
	v_lshlrev_b64 v[4:5], 14, v[4:5]
	s_ashr_i32 s9, s8, 31
	v_lshl_add_u64 v[4:5], s[0:1], 0, v[4:5]
	v_cndmask_b32_e64 v6, 0, 1, s[4:5]
	v_lshl_add_u64 v[4:5], s[8:9], 2, v[4:5]
	v_mov_b32_e32 v160, 1.0
	v_mov_b32_e32 v158, 1.0
	v_mov_b32_e32 v156, 1.0
	v_mov_b32_e32 v154, 1.0
	v_mov_b32_e32 v152, 1.0
	v_mov_b32_e32 v150, 1.0
	v_mov_b32_e32 v148, 1.0
	v_mov_b32_e32 v146, 1.0
	v_mov_b32_e32 v144, 1.0
	v_mov_b32_e32 v142, 1.0
	v_mov_b32_e32 v140, 1.0
	v_mov_b32_e32 v138, 1.0
	v_mov_b32_e32 v136, 1.0
	v_mov_b32_e32 v134, 1.0
	v_mov_b32_e32 v132, 1.0
	v_mov_b32_e32 v130, 1.0
	v_cmp_ne_u32_e64 s[2:3], 1, v6
	s_andn2_b64 vcc, exec, s[4:5]
	s_cbranch_vccnz .LBB0_388
	global_load_dwordx4 v[188:191], v[4:5], off
	global_load_dwordx4 v[192:195], v[4:5], off offset:16
	global_load_dwordx4 v[196:199], v[4:5], off offset:32
	global_load_dwordx4 v[200:203], v[4:5], off offset:48
	s_waitcnt vmcnt(0)
	v_mul_f32_e32 v160, 0x3db504f3, v188
	v_mul_f32_e32 v158, 0x3db504f3, v189
	v_mul_f32_e32 v156, 0x3db504f3, v190
	v_mul_f32_e32 v154, 0x3db504f3, v191
	v_mul_f32_e32 v152, 0x3db504f3, v192
	v_mul_f32_e32 v150, 0x3db504f3, v193
	v_mul_f32_e32 v148, 0x3db504f3, v194
	v_mul_f32_e32 v146, 0x3db504f3, v195
	v_mul_f32_e32 v144, 0x3db504f3, v196
	v_mul_f32_e32 v142, 0x3db504f3, v197
	v_mul_f32_e32 v140, 0x3db504f3, v198
	v_mul_f32_e32 v138, 0x3db504f3, v199
	v_mul_f32_e32 v136, 0x3db504f3, v200
	v_mul_f32_e32 v134, 0x3db504f3, v201
	v_mul_f32_e32 v132, 0x3db504f3, v202
	v_mul_f32_e32 v130, 0x3db504f3, v203
	s_branch .LBB0_388

.LBB0_549:
	s_add_i32 s0, s77, 0x26b28
	v_mov_b32_e32 v6, s0
	s_add_i32 s0, s77, 0x26b2c
	v_mov_b32_e32 v7, s0
	ds_read_b32 v6, v6
	ds_read_b32 v7, v7
	s_cmp_lg_u32 s4, 0
	s_waitcnt lgkmcnt(1)
	v_readfirstlane_b32 s1, v6
	s_waitcnt lgkmcnt(0)
	v_readfirstlane_b32 s0, v7
	s_cbranch_scc0 .LBB0_617
	v_writelane_b32 v255, s70, 23
	s_lshl_b32 s4, s4, 2
	v_lshlrev_b32_e32 v160, 4, v5
	v_writelane_b32 v255, s71, 24
	v_writelane_b32 v255, s4, 20
	s_add_u32 s4, s3, 0x1da00000
	v_writelane_b32 v255, s4, 43
	s_addc_u32 s4, s2, 0
	v_writelane_b32 v255, s4, 44
	s_add_u32 s9, s3, 0x2da00000
	v_readlane_b32 s16, v255, 6
	v_readlane_b32 s17, v255, 7
	s_addc_u32 s10, s2, 0
	s_lshl_b64 s[4:5], s[16:17], 10
	s_add_u32 s4, s1, s4
	s_addc_u32 s5, s0, s5
	s_waitcnt vmcnt(0) lgkmcnt(0)
	s_barrier
	v_lshl_add_u64 v[6:7], s[4:5], 0, v[160:161]
	flat_load_dwordx4 v[6:9], v[6:7]
	v_readlane_b32 s1, v255, 18
	s_lshl_b32 s0, s1, 6
	s_lshl_b32 s1, s1, 8
	s_and_b32 s4, s0, 0xfffff000
	s_and_b32 s1, s1, 0x700
	s_or_b32 s1, s1, s4
	s_xor_b32 s1, s1, 0xf00
	s_mul_hi_i32 s7, s1, 0x6800
	s_mulk_i32 s1, 0x6800
	s_add_u32 s1, s9, s1
	s_addc_u32 s7, s10, s7
	s_and_b32 s0, s0, 0xe00
	s_add_u32 s8, s1, s0
	s_mul_hi_i32 s5, s4, 0x6800
	s_mulk_i32 s4, 0x6800
	s_addc_u32 s7, s7, 0
	s_add_u32 s1, s9, s4
	s_addc_u32 s4, s10, s5
	s_add_u32 s5, s1, s0
	v_writelane_b32 v255, s9, 21
	s_addc_u32 s9, s4, 0
	s_add_u32 s0, s5, 0x2800
	v_add_u32_e32 v165, s67, v0
	s_addc_u32 s1, s9, 0
	v_readfirstlane_b32 s6, v165
	s_add_u32 s4, s5, 0x3800
	v_and_b32_e32 v10, 31, v0
	s_addc_u32 s5, s9, 0
	s_ashr_i32 s6, s6, 6
	v_lshrrev_b32_e32 v12, 1, v0
	v_lshrrev_b32_e32 v5, 4, v5
	v_and_b32_e32 v14, 15, v0
	v_bfe_u32 v17, v0, 2, 3
	v_lshlrev_b32_e32 v16, 3, v0
	v_mul_u32_u24_e32 v10, 0x6800, v10
	v_writelane_b32 v255, s10, 22
	s_lshl_b32 s9, s6, 3
	s_lshl_b32 s10, s6, 2
	v_and_b32_e32 v18, 32, v0
	v_bitop3_b32 v0, v5, v0, 15 bitop3:0x78
	v_bitop3_b32 v14, v5, v14, 4 bitop3:0x36
	v_and_b32_e32 v19, 8, v12
	v_and_b32_e32 v20, 24, v16
	v_and_or_b32 v16, v12, 16, v10
	v_or_b32_e32 v5, s9, v5
	v_bitop3_b32 v10, s9, v228, v17 bitop3:0xc8
	s_and_b32 s9, s10, 4
	v_mul_lo_u32 v5, v5, s84
	v_or3_b32 v12, v19, v10, s9
	v_lshl_or_b32 v10, v0, 4, v5
	v_lshl_or_b32 v0, v14, 4, v5
	v_mul_u32_u24_e32 v5, 0x3400, v12
	s_add_i32 s13, s77, 0x18100
	v_add_u32_e32 v12, 0x1a000, v0
	v_or3_b32 v0, v18, v20, v5
	v_mov_b32_e32 v11, v161
	v_mov_b32_e32 v13, v161
	v_mov_b32_e32 v15, v161
	v_add_u32_e32 v24, s13, v160
	v_lshlrev_b32_e32 v14, 1, v0
	s_add_i32 s14, s77, 0x10000
	s_lshl_b32 s11, s6, 11
	v_lshl_add_u64 v[10:11], s[0:1], 0, v[10:11]
	v_lshl_add_u64 v[12:13], s[0:1], 0, v[12:13]
	v_lshl_add_u64 v[14:15], s[4:5], 0, v[14:15]
	s_mov_b64 s[0:1], 0x180
	s_add_i32 s10, s11, s14
	v_lshl_add_u64 v[22:23], v[14:15], 0, s[0:1]
	s_lshl_b32 s12, s6, 12
	s_add_i32 s9, s10, 0x400
	v_writelane_b32 v255, s13, 28
	s_lshl_b32 s13, s6, 5
	s_add_i32 s11, s12, s77
	s_mul_hi_i32 s12, s13, 0x6800
	s_add_i32 s13, s11, 0x400
	v_lshl_add_u64 v[18:19], v[14:15], 0, s[86:87]
	v_writelane_b32 v255, s14, 53
	s_add_i32 s14, s11, 0x800
	v_lshl_add_u64 v[20:21], v[14:15], 0, s[62:63]
	s_waitcnt vmcnt(0) lgkmcnt(0)
	ds_write_b128 v24, v[6:9]
	s_mov_b32 s0, m0
	s_mov_b32 m0, s10
	s_nop 0
	global_load_lds_dwordx4 v[10:11], off
	s_mov_b32 m0, s0
	s_mul_i32 s6, s6, 0xd0000
	s_mov_b32 s0, m0
	s_mov_b32 m0, s9
	s_nop 0
	global_load_lds_dwordx4 v[12:13], off
	s_mov_b32 m0, s0
	s_add_i32 s15, s11, 0xc00
	s_mov_b32 s0, m0
	s_mov_b32 m0, s11
	s_nop 0
	global_load_lds_dwordx4 v[14:15], off
	s_mov_b32 m0, s0
	v_mov_b32_e32 v17, v161
	s_mov_b32 s0, m0
	s_mov_b32 m0, s13
	s_nop 0
	global_load_lds_dwordx4 v[18:19], off
	s_mov_b32 m0, s0
	v_cvt_f32_u32_e32 v0, s16
	s_mov_b32 s0, m0
	s_mov_b32 m0, s14
	s_nop 0
	global_load_lds_dwordx4 v[20:21], off
	s_mov_b32 m0, s0
	s_mov_b64 s[80:81], src_shared_base
	s_mov_b32 s0, m0
	s_mov_b32 m0, s15
	s_nop 0
	global_load_lds_dwordx4 v[22:23], off
	s_mov_b32 m0, s0
	s_add_u32 s0, s8, s6
	s_addc_u32 s1, s7, s12
	s_add_u32 s0, s0, 0x1800
	s_addc_u32 s1, s1, 0
	v_lshl_add_u64 v[6:7], s[0:1], 0, v[16:17]
	flat_load_dwordx4 v[128:131], v[6:7]
	flat_load_dwordx4 v[132:135], v[6:7] offset:32
	flat_load_dwordx4 v[136:139], v[6:7] offset:64
	flat_load_dwordx4 v[140:143], v[6:7] offset:96
	flat_load_dwordx4 v[144:147], v[6:7] offset:128
	flat_load_dwordx4 v[148:151], v[6:7] offset:160
	flat_load_dwordx4 v[152:155], v[6:7] offset:192
	flat_load_dwordx4 v[166:169], v[6:7] offset:224
	v_cmp_eq_u32_e64 s[0:1], 0, v165
	s_add_i32 s4, s77, 0x18800
	s_mov_b32 s5, s81
	v_writelane_b32 v255, s0, 49
	v_mul_f32_e32 v0, 0xbe99999a, v0
	v_mul_f32_e32 v0, 0x3fb8aa3b, v0
	v_writelane_b32 v255, s1, 50
	v_writelane_b32 v255, s4, 46
	v_exp_f32_e32 v0, v0
	v_add_f32_e32 v1, v1, v3
	v_writelane_b32 v255, s5, 47
	s_add_i32 s4, s77, 0x18820
	v_add_f32_e32 v2, v2, v4
	v_writelane_b32 v255, s4, 51
	s_add_i32 s4, s77, 0x14000
	v_mul_f32_e32 v1, 0x3fb8aa3b, v1
	v_mul_f32_e32 v2, 0x3fb8aa3b, v2
	v_writelane_b32 v255, s4, 56
	s_add_i32 s4, s77, 0x18804
	s_mov_b32 s5, s81
	v_exp_f32_e32 v1, v1
	v_exp_f32_e32 v2, v2
	s_add_i32 s0, s77, 0x18810
	s_add_i32 s80, s77, 0x18808
	s_add_i32 s72, s77, 0x1880c
	s_add_i32 s70, s77, 0x18814
	v_writelane_b32 v255, s4, 54
	v_mov_b32_e32 v3, 0xbf4ccccd
	s_add_u32 s3, s3, 0x2dd43800
	v_writelane_b32 v255, s5, 55
	v_fmamk_f32 v0, v0, 0x3f19999a, v3
	v_writelane_b32 v255, s3, 27
	s_addc_u32 s2, s2, 0
	v_add_f32_e32 v173, 1.0, v0
	v_writelane_b32 v255, s2, 29
	v_sub_f32_e32 v0, v1, v2
	v_sub_f32_e32 v1, 1.0, v173
	v_writelane_b32 v255, s77, 48
	v_add_f32_e32 v174, v1, v0
	s_mov_b32 s94, 0
	s_mov_b32 s1, s81
	s_mov_b32 s73, s81
	s_mov_b32 s71, s81
	v_writelane_b32 v255, s18, 19
	s_waitcnt vmcnt(0)
	s_branch .LBB0_552

.LBB0_552:
	s_lshr_b32 s2, s94, 2
	s_mul_i32 s2, s18, s2
	v_readlane_b32 s3, v255, 18
	s_add_i32 s2, s3, s2
	s_lshl_b32 s4, s2, 8
	s_lshl_b32 s68, s2, 6
	s_and_b32 s4, s4, 0x700
	s_and_b32 s3, s94, 2
	s_and_b32 s74, s68, 0xfffff000
	s_xor_b32 s5, s4, 0xf00
	s_cmp_eq_u32 s3, 0
	s_cselect_b32 s78, s5, s4
	v_writelane_b32 v255, s94, 25
	s_or_b32 s94, s78, s74
	s_mul_i32 s4, s94, 0x6800
	v_readlane_b32 s5, v255, 21
	s_mul_hi_i32 s3, s94, 0x6800
	s_add_u32 s4, s5, s4
	v_readlane_b32 s6, v255, 22
	s_addc_u32 s3, s6, s3
	s_lshl_b32 s2, s2, 5
	s_and_b32 s2, s2, 0x700
	s_lshl_b32 s16, s2, 1
	s_add_u32 s2, s4, s16
	s_addc_u32 s3, s3, 0
	s_add_u32 s12, s2, 0x1800
	s_addc_u32 s13, s3, 0
	s_mul_hi_i32 s69, s74, 0x6800
	s_mulk_i32 s74, 0x6800
	s_add_u32 s2, s5, s74
	s_addc_u32 s3, s6, s69
	s_add_u32 s14, s2, s16
	s_addc_u32 s15, s3, 0
	s_add_u32 s66, s14, 0x3800
	s_addc_u32 s67, s15, 0
	s_mov_b64 s[4:5], exec
	v_readlane_b32 s6, v255, 49
	v_readlane_b32 s7, v255, 50
	s_and_b64 s[6:7], s[4:5], s[6:7]
	s_mov_b64 exec, s[6:7]
	s_cbranch_execz .LBB0_554
	s_add_u32 s6, s14, 0x2900
	s_addc_u32 s7, s15, 0
	s_add_u32 s8, s12, 0x100
	v_readlane_b32 s10, v255, 46
	s_addc_u32 s9, s13, 0
	v_readlane_b32 s11, v255, 47
	v_mov_b64_e32 v[2:3], s[8:9]
	s_nop 0
	v_mov_b64_e32 v[0:1], s[10:11]
	ds_write_b64 v0, v[2:3]
	s_waitcnt lgkmcnt(0)
	v_mov_b64_e32 v[0:1], s[80:81]
	v_mov_b64_e32 v[2:3], s[6:7]
	ds_write_b64 v0, v[2:3]
	s_waitcnt lgkmcnt(0)
	v_mov_b64_e32 v[0:1], s[0:1]
	v_mov_b64_e32 v[2:3], s[66:67]
	ds_write_b64 v0, v[2:3]
	s_waitcnt lgkmcnt(0)
.LBB0_554:
	s_or_b64 exec, exec, s[4:5]
	s_ashr_i32 s95, s94, 31
	s_add_u32 s4, s2, s16
	s_addc_u32 s3, s3, 0
	v_mov_b32_e32 v38, v165
	s_add_u32 s2, s4, 0x2800
	s_addc_u32 s33, s3, 0
	v_readfirstlane_b32 s5, v38
	s_ashr_i32 s79, s5, 6
	v_bfe_u32 v0, v38, 5, 1
	v_and_b32_e32 v175, 31, v38
	s_lshl_b32 s92, s79, 5
	v_lshlrev_b32_e32 v32, 2, v0
	s_add_i32 s82, s92, s78
	v_sub_u32_e32 v1, v175, v32
	v_lshlrev_b32_e32 v176, 4, v0
	s_lshl_b32 s76, s79, 3
	v_bfe_u32 v0, v38, 4, 2
	v_writelane_b32 v255, s16, 17
	v_add_u32_e32 v179, s82, v1
	v_or_b32_e32 v1, s76, v0
	v_and_b32_e32 v2, 15, v38
	s_lshl_b32 s5, s79, 12
	v_and_b32_e32 v39, 63, v38
	v_bitop3_b32 v3, v0, v38, 15 bitop3:0x78
	v_mul_lo_u32 v1, v1, s84
	v_bitop3_b32 v0, v0, v2, 4 bitop3:0x36
	s_add_i32 s93, s5, s77
	s_mul_i32 s5, s79, 0x1c00
	v_readlane_b32 s7, v255, 51
	s_waitcnt vmcnt(16)
	v_lshlrev_b32_e32 v40, 4, v39
	v_lshl_or_b32 v0, v0, 4, v1
	s_lshl_b32 s83, s79, 11
	v_readlane_b32 s6, v255, 53
	s_add_i32 s5, s7, s5
	v_lshl_or_b32 v160, v3, 4, v1
	v_add_u32_e32 v170, 0x1a000, v0
	s_add_i32 s83, s83, s6
	v_add_u32_e32 v180, s5, v40
	s_waitcnt vmcnt(16) lgkmcnt(0)
	ds_write_b128 v180, v[128:131]
	ds_write_b128 v180, v[132:135] offset:1024
	ds_write_b128 v180, v[136:139] offset:2048
	ds_write_b128 v180, v[140:143] offset:3072
	ds_write_b128 v180, v[144:147] offset:4096
	ds_write_b128 v180, v[148:151] offset:5120
	ds_write_b128 v180, v[152:155] offset:6144
	s_add_u32 s4, s4, 0x1a2800
	s_addc_u32 s5, s3, 0
	v_lshl_add_u64 v[0:1], s[4:5], 0, v[160:161]
	s_add_i32 s84, s83, 0x4000
	s_mov_b32 s3, m0
	s_mov_b32 m0, s84
	s_nop 0
	global_load_lds_dwordx4 v[0:1], off
	s_mov_b32 m0, s3
	v_mov_b32_e32 v171, v161
	v_lshl_add_u64 v[0:1], s[4:5], 0, v[170:171]
	s_add_i32 s85, s83, 0x4400
	s_mov_b32 s3, m0
	s_mov_b32 m0, s85
	s_nop 0
	global_load_lds_dwordx4 v[0:1], off
	s_mov_b32 m0, s3
	s_waitcnt lgkmcnt(0)
	s_barrier
	v_lshlrev_b32_e32 v0, 4, v38
	s_movk_i32 s3, 0x70
	v_lshlrev_b32_e32 v33, 8, v175
	v_and_b32_e32 v1, 0x70, v0
	v_bitop3_b32 v34, v176, v0, s3 bitop3:0x78
	s_movk_i32 s3, 0x60
	v_add_u32_e32 v2, s6, v33
	v_bitop3_b32 v35, v176, v1, 32 bitop3:0x36
	v_bitop3_b32 v36, v176, v1, 64 bitop3:0x36
	v_bitop3_b32 v37, v176, v1, s3 bitop3:0x36
	v_add_u32_e32 v181, v34, v2
	v_add_u32_e32 v182, v35, v2
	v_add_u32_e32 v183, v36, v2
	v_add_u32_e32 v184, v37, v2
	ds_read_b128 v[0:3], v181 offset:0
	ds_read_b128 v[4:7], v181 offset:0x2000
	ds_read_b128 v[8:11], v180 offset:0
	ds_read_b128 v[42:45], v182 offset:0
	ds_read_b128 v[46:49], v182 offset:0x2000
	ds_read_b128 v[50:53], v180 offset:0x400
	s_waitcnt lgkmcnt(3)
	s_nop 0
	v_mfma_f32_32x32x16_bf16 v[16:31], v[0:3], v[8:11], 0
	v_mfma_f32_32x32x16_bf16 v[0:15], v[4:7], v[8:11], 0
	ds_read_b128 v[54:57], v183 offset:0
	ds_read_b128 v[58:61], v183 offset:0x2000
	ds_read_b128 v[62:65], v180 offset:0x800
	s_waitcnt lgkmcnt(3)
	v_mfma_f32_32x32x16_bf16 v[16:31], v[42:45], v[50:53], v[16:31]
	v_mfma_f32_32x32x16_bf16 v[0:15], v[46:49], v[50:53], v[0:15]
	ds_read_b128 v[42:45], v184 offset:0
	ds_read_b128 v[46:49], v184 offset:0x2000
	ds_read_b128 v[50:53], v180 offset:0xc00
	s_waitcnt lgkmcnt(3)
	v_mfma_f32_32x32x16_bf16 v[16:31], v[54:57], v[62:65], v[16:31]
	v_mfma_f32_32x32x16_bf16 v[0:15], v[58:61], v[62:65], v[0:15]
	ds_read_b128 v[54:57], v181 offset:0x80
	ds_read_b128 v[58:61], v181 offset:0x2080
	ds_read_b128 v[62:65], v180 offset:0x1000
	s_waitcnt lgkmcnt(3)
	v_mfma_f32_32x32x16_bf16 v[16:31], v[42:45], v[50:53], v[16:31]
	v_mfma_f32_32x32x16_bf16 v[0:15], v[46:49], v[50:53], v[0:15]
	ds_read_b128 v[42:45], v182 offset:0x80
	ds_read_b128 v[46:49], v182 offset:0x2080
	ds_read_b128 v[50:53], v180 offset:0x1400
	s_waitcnt lgkmcnt(3)
	v_mfma_f32_32x32x16_bf16 v[16:31], v[54:57], v[62:65], v[16:31]
	v_mfma_f32_32x32x16_bf16 v[0:15], v[58:61], v[62:65], v[0:15]
	ds_read_b128 v[54:57], v183 offset:0x80
	ds_read_b128 v[58:61], v183 offset:0x2080
	ds_read_b128 v[62:65], v180 offset:0x1800
	s_waitcnt lgkmcnt(3)
	v_mfma_f32_32x32x16_bf16 v[16:31], v[42:45], v[50:53], v[16:31]
	v_mfma_f32_32x32x16_bf16 v[0:15], v[46:49], v[50:53], v[0:15]
	ds_read_b128 v[42:45], v184 offset:0x80
	ds_read_b128 v[46:49], v184 offset:0x2080
	s_waitcnt lgkmcnt(2)
	v_mfma_f32_32x32x16_bf16 v[16:31], v[54:57], v[62:65], v[16:31]
	v_mfma_f32_32x32x16_bf16 v[0:15], v[58:61], v[62:65], v[0:15]
	s_waitcnt lgkmcnt(0)
	v_mfma_f32_32x32x16_bf16 v[16:31], v[42:45], v[166:169], v[16:31]
	v_mfma_f32_32x32x16_bf16 v[0:15], v[46:49], v[166:169], v[0:15]
	s_bitcmp0_b32 s100, 8
	s_cbranch_scc1 .Lstg_a9
	s_waitcnt vmcnt(0)
	s_waitcnt lgkmcnt(0)
	s_barrier

.LBB0_584:
	s_lshl_b64 s[2:3], s[94:95], 12
	v_readlane_b32 s4, v255, 43
	s_add_u32 s2, s4, s2
	v_readlane_b32 s4, v255, 44
	s_addc_u32 s3, s4, s3
	v_readlane_b32 s4, v255, 17
	s_add_u32 s83, s2, s4
	s_addc_u32 s95, s3, 0
	v_add_f32_e32 v162, v144, v145
	v_fmac_f32_e32 v162, v178, v160
	v_mul_u32_u24_e32 v160, 0x6800, v175
	ds_read_b64_tr_b16 v[144:145], v177 offset:0x8000
	ds_read_b64_tr_b16 v[146:147], v177 offset:0x9000
	ds_read_b64_tr_b16 v[148:149], v177 offset:0xa000
	ds_read_b64_tr_b16 v[150:151], v177 offset:0xb000
	ds_read_b64_tr_b16 v[152:153], v177 offset:0xc000
	ds_read_b64_tr_b16 v[154:155], v177 offset:0xd000
	ds_read_b64_tr_b16 v[156:157], v177 offset:0xe000
	ds_read_b64_tr_b16 v[158:159], v177 offset:0xf000
	ds_read_b64_tr_b16 v[166:167], v177 offset:0x8200
	ds_read_b64_tr_b16 v[168:169], v177 offset:0x9200
	ds_read_b64_tr_b16 v[178:179], v177 offset:0xa200
	ds_read_b64_tr_b16 v[180:181], v177 offset:0xb200
	ds_read_b64_tr_b16 v[182:183], v177 offset:0xc200
	ds_read_b64_tr_b16 v[184:185], v177 offset:0xd200
	ds_read_b64_tr_b16 v[186:187], v177 offset:0xe200
	ds_read_b64_tr_b16 v[188:189], v177 offset:0xf200
	s_waitcnt lgkmcnt(8)
	s_nop 0
	v_mfma_f32_32x32x16_bf16 v[112:127], v[144:147], v[128:131], v[112:127]
	v_mfma_f32_32x32x16_bf16 v[112:127], v[148:151], v[132:135], v[112:127]
	v_mfma_f32_32x32x16_bf16 v[112:127], v[152:155], v[136:139], v[112:127]
	v_mfma_f32_32x32x16_bf16 v[112:127], v[156:159], v[140:143], v[112:127]
	ds_read_b64_tr_b16 v[144:145], v177 offset:0x8400
	ds_read_b64_tr_b16 v[146:147], v177 offset:0x9400
	ds_read_b64_tr_b16 v[148:149], v177 offset:0xa400
	ds_read_b64_tr_b16 v[150:151], v177 offset:0xb400
	ds_read_b64_tr_b16 v[152:153], v177 offset:0xc400
	ds_read_b64_tr_b16 v[154:155], v177 offset:0xd400
	ds_read_b64_tr_b16 v[156:157], v177 offset:0xe400
	ds_read_b64_tr_b16 v[158:159], v177 offset:0xf400
	s_waitcnt lgkmcnt(8)
	v_mfma_f32_32x32x16_bf16 v[80:95], v[166:169], v[128:131], v[80:95]
	v_mfma_f32_32x32x16_bf16 v[80:95], v[178:181], v[132:135], v[80:95]
	v_mfma_f32_32x32x16_bf16 v[80:95], v[182:185], v[136:139], v[80:95]
	v_mfma_f32_32x32x16_bf16 v[80:95], v[186:189], v[140:143], v[80:95]
	ds_read_b64_tr_b16 v[166:167], v177 offset:0x8600
	ds_read_b64_tr_b16 v[168:169], v177 offset:0x9600
	ds_read_b64_tr_b16 v[178:179], v177 offset:0xa600
	ds_read_b64_tr_b16 v[180:181], v177 offset:0xb600
	ds_read_b64_tr_b16 v[182:183], v177 offset:0xc600
	ds_read_b64_tr_b16 v[184:185], v177 offset:0xd600
	ds_read_b64_tr_b16 v[186:187], v177 offset:0xe600
	ds_read_b64_tr_b16 v[188:189], v177 offset:0xf600
	s_waitcnt lgkmcnt(8)
	v_mfma_f32_32x32x16_bf16 v[96:111], v[144:147], v[128:131], v[96:111]
	v_mfma_f32_32x32x16_bf16 v[96:111], v[148:151], v[132:135], v[96:111]
	v_mfma_f32_32x32x16_bf16 v[96:111], v[152:155], v[136:139], v[96:111]
	v_mfma_f32_32x32x16_bf16 v[96:111], v[156:159], v[140:143], v[96:111]
	ds_read_b64_tr_b16 v[144:145], v177 offset:0x8800
	ds_read_b64_tr_b16 v[146:147], v177 offset:0x9800
	ds_read_b64_tr_b16 v[148:149], v177 offset:0xa800
	ds_read_b64_tr_b16 v[150:151], v177 offset:0xb800
	ds_read_b64_tr_b16 v[152:153], v177 offset:0xc800
	ds_read_b64_tr_b16 v[154:155], v177 offset:0xd800
	ds_read_b64_tr_b16 v[156:157], v177 offset:0xe800
	ds_read_b64_tr_b16 v[158:159], v177 offset:0xf800
	s_waitcnt lgkmcnt(8)
	v_mfma_f32_32x32x16_bf16 v[64:79], v[166:169], v[128:131], v[64:79]
	v_mfma_f32_32x32x16_bf16 v[64:79], v[178:181], v[132:135], v[64:79]
	v_mfma_f32_32x32x16_bf16 v[64:79], v[182:185], v[136:139], v[64:79]
	v_mfma_f32_32x32x16_bf16 v[64:79], v[186:189], v[140:143], v[64:79]
	ds_read_b64_tr_b16 v[166:167], v177 offset:0x8a00
	ds_read_b64_tr_b16 v[168:169], v177 offset:0x9a00
	ds_read_b64_tr_b16 v[178:179], v177 offset:0xaa00
	ds_read_b64_tr_b16 v[180:181], v177 offset:0xba00
	ds_read_b64_tr_b16 v[182:183], v177 offset:0xca00
	ds_read_b64_tr_b16 v[184:185], v177 offset:0xda00
	ds_read_b64_tr_b16 v[186:187], v177 offset:0xea00
	ds_read_b64_tr_b16 v[188:189], v177 offset:0xfa00
	s_waitcnt lgkmcnt(8)
	v_mfma_f32_32x32x16_bf16 v[48:63], v[144:147], v[128:131], v[48:63]
	v_mfma_f32_32x32x16_bf16 v[48:63], v[148:151], v[132:135], v[48:63]
	v_mfma_f32_32x32x16_bf16 v[48:63], v[152:155], v[136:139], v[48:63]
	v_mfma_f32_32x32x16_bf16 v[48:63], v[156:159], v[140:143], v[48:63]
	ds_read_b64_tr_b16 v[144:145], v177 offset:0x8c00
	ds_read_b64_tr_b16 v[146:147], v177 offset:0x9c00
	ds_read_b64_tr_b16 v[148:149], v177 offset:0xac00
	ds_read_b64_tr_b16 v[150:151], v177 offset:0xbc00
	ds_read_b64_tr_b16 v[152:153], v177 offset:0xcc00
	ds_read_b64_tr_b16 v[154:155], v177 offset:0xdc00
	ds_read_b64_tr_b16 v[156:157], v177 offset:0xec00
	ds_read_b64_tr_b16 v[158:159], v177 offset:0xfc00
	s_waitcnt lgkmcnt(8)
	v_mfma_f32_32x32x16_bf16 v[32:47], v[166:169], v[128:131], v[32:47]
	v_mfma_f32_32x32x16_bf16 v[32:47], v[178:181], v[132:135], v[32:47]
	v_mfma_f32_32x32x16_bf16 v[32:47], v[182:185], v[136:139], v[32:47]
	v_mfma_f32_32x32x16_bf16 v[32:47], v[186:189], v[140:143], v[32:47]
	ds_read_b64_tr_b16 v[166:167], v177 offset:0x8e00
	ds_read_b64_tr_b16 v[168:169], v177 offset:0x9e00
	ds_read_b64_tr_b16 v[178:179], v177 offset:0xae00
	ds_read_b64_tr_b16 v[180:181], v177 offset:0xbe00
	ds_read_b64_tr_b16 v[182:183], v177 offset:0xce00
	ds_read_b64_tr_b16 v[184:185], v177 offset:0xde00
	ds_read_b64_tr_b16 v[186:187], v177 offset:0xee00
	ds_read_b64_tr_b16 v[188:189], v177 offset:0xfe00
	s_waitcnt lgkmcnt(8)
	v_mfma_f32_32x32x16_bf16 v[16:31], v[144:147], v[128:131], v[16:31]
	v_mfma_f32_32x32x16_bf16 v[16:31], v[148:151], v[132:135], v[16:31]
	v_mfma_f32_32x32x16_bf16 v[16:31], v[152:155], v[136:139], v[16:31]
	v_mfma_f32_32x32x16_bf16 v[16:31], v[156:159], v[140:143], v[16:31]
	s_waitcnt lgkmcnt(0)
	v_mfma_f32_32x32x16_bf16 v[0:15], v[166:169], v[128:131], v[0:15]
	v_mfma_f32_32x32x16_bf16 v[0:15], v[178:181], v[132:135], v[0:15]
	v_mfma_f32_32x32x16_bf16 v[0:15], v[182:185], v[136:139], v[0:15]
	v_mfma_f32_32x32x16_bf16 v[0:15], v[186:189], v[140:143], v[0:15]
	v_readlane_b32 s2, v255, 46
	v_readlane_b32 s3, v255, 47
	s_ashr_i32 s93, s92, 31
	v_or_b32_e32 v160, v176, v160
	v_mov_b64_e32 v[128:129], s[2:3]
	v_readlane_b32 s2, v255, 54
	v_readlane_b32 s3, v255, 55
	flat_load_dword v130, v[128:129] sc0 sc1
	s_waitcnt vmcnt(0) lgkmcnt(0)
	v_readfirstlane_b32 s5, v130
	v_mov_b64_e32 v[128:129], s[2:3]
	flat_load_dword v128, v[128:129] sc0 sc1
	s_waitcnt vmcnt(0)
	s_mul_i32 s2, s92, 0x6800
	s_mul_hi_i32 s3, s92, 0x6800
	s_add_u32 s2, s5, s2
	s_waitcnt lgkmcnt(0)
	s_barrier
	s_waitcnt lgkmcnt(0)
	v_readfirstlane_b32 s4, v128
	s_addc_u32 s3, s4, s3
	v_lshl_add_u64 v[156:157], s[2:3], 0, v[160:161]
	flat_load_dwordx4 v[128:131], v[156:157]
	flat_load_dwordx4 v[132:135], v[156:157] offset:32
	flat_load_dwordx4 v[136:139], v[156:157] offset:64
	flat_load_dwordx4 v[140:143], v[156:157] offset:96
	flat_load_dwordx4 v[144:147], v[156:157] offset:128
	flat_load_dwordx4 v[148:151], v[156:157] offset:160
	flat_load_dwordx4 v[152:155], v[156:157] offset:192
	flat_load_dwordx4 v[166:169], v[156:157] offset:224
	v_rcp_f32_e32 v156, v162
	s_lshl_b64 s[2:3], s[92:93], 12
	s_add_u32 s4, s83, s2
	s_addc_u32 s5, s95, s3
	v_mul_f32_e32 v80, v156, v80
	v_mul_f32_e32 v81, v156, v81
	v_cvt_pk_f16_f32 v80, v80, v81
	v_mul_f32_e32 v81, v156, v82
	v_mul_f32_e32 v82, v156, v83
	v_cvt_pk_f16_f32 v81, v81, v82
	v_mul_f32_e32 v82, v156, v84
	v_mul_f32_e32 v83, v156, v85
	v_cvt_pk_f16_f32 v82, v82, v83
	v_mul_f32_e32 v83, v156, v86
	v_mul_f32_e32 v84, v156, v87
	v_cvt_pk_f16_f32 v83, v83, v84
	v_lshl_or_b32 v157, v175, 12, v176
	v_permlane32_swap_b32_e32 v80, v82
	v_permlane32_swap_b32_e32 v81, v83
	global_store_dwordx4 v157, v[80:83], s[4:5] offset:64
	v_mul_f32_e32 v84, v156, v95
	v_mul_f32_e32 v112, v156, v112
	v_mul_f32_e32 v80, v156, v88
	v_mul_f32_e32 v81, v156, v89
	v_cvt_pk_f16_f32 v80, v80, v81
	v_mul_f32_e32 v81, v156, v90
	v_mul_f32_e32 v82, v156, v91
	v_cvt_pk_f16_f32 v81, v81, v82
	v_mul_f32_e32 v82, v156, v92
	v_mul_f32_e32 v83, v156, v93
	v_cvt_pk_f16_f32 v82, v82, v83
	v_mul_f32_e32 v83, v156, v94
	v_cvt_pk_f16_f32 v83, v83, v84
	v_permlane32_swap_b32_e32 v80, v82
	s_nop 0
	v_permlane32_swap_b32_e32 v81, v83
	v_mul_f32_e32 v113, v156, v113
	global_store_dwordx4 v157, v[80:83], s[4:5] offset:96
	v_mul_f32_e32 v64, v156, v64
	v_mul_f32_e32 v65, v156, v65
	v_mul_f32_e32 v80, v156, v96
	v_mul_f32_e32 v81, v156, v97
	v_mul_f32_e32 v48, v156, v48
	v_mul_f32_e32 v49, v156, v49
	v_mul_f32_e32 v32, v156, v32
	v_mul_f32_e32 v33, v156, v33
	v_mul_f32_e32 v16, v156, v16
	v_mul_f32_e32 v17, v156, v17
	v_mul_f32_e32 v0, v156, v0
	v_mul_f32_e32 v1, v156, v1
	v_cvt_pk_f16_f32 v112, v112, v113
	v_mul_f32_e32 v113, v156, v114
	v_mul_f32_e32 v114, v156, v115
	v_cvt_pk_f16_f32 v80, v80, v81
	v_mul_f32_e32 v81, v156, v98
	v_mul_f32_e32 v82, v156, v99
	v_cvt_pk_f16_f32 v64, v64, v65
	v_mul_f32_e32 v65, v156, v66
	v_mul_f32_e32 v66, v156, v67
	v_cvt_pk_f16_f32 v48, v48, v49
	v_mul_f32_e32 v49, v156, v50
	v_mul_f32_e32 v50, v156, v51
	v_cvt_pk_f16_f32 v32, v32, v33
	v_mul_f32_e32 v33, v156, v34
	v_mul_f32_e32 v34, v156, v35
	v_cvt_pk_f16_f32 v16, v16, v17
	v_mul_f32_e32 v17, v156, v18
	v_mul_f32_e32 v18, v156, v19
	v_cvt_pk_f16_f32 v0, v0, v1
	v_mul_f32_e32 v1, v156, v2
	v_mul_f32_e32 v2, v156, v3
	v_cvt_pk_f16_f32 v113, v113, v114
	v_mul_f32_e32 v114, v156, v116
	v_mul_f32_e32 v115, v156, v117
	v_cvt_pk_f16_f32 v81, v81, v82
	v_mul_f32_e32 v82, v156, v100
	v_mul_f32_e32 v83, v156, v101
	v_cvt_pk_f16_f32 v65, v65, v66
	v_mul_f32_e32 v66, v156, v68
	v_mul_f32_e32 v67, v156, v69
	v_cvt_pk_f16_f32 v49, v49, v50
	v_mul_f32_e32 v50, v156, v52
	v_mul_f32_e32 v51, v156, v53
	v_cvt_pk_f16_f32 v33, v33, v34
	v_mul_f32_e32 v34, v156, v36
	v_mul_f32_e32 v35, v156, v37
	v_cvt_pk_f16_f32 v17, v17, v18
	v_mul_f32_e32 v18, v156, v20
	v_mul_f32_e32 v19, v156, v21
	v_cvt_pk_f16_f32 v1, v1, v2
	v_mul_f32_e32 v2, v156, v4
	v_mul_f32_e32 v3, v156, v5
	v_cvt_pk_f16_f32 v114, v114, v115
	v_mul_f32_e32 v115, v156, v118
	v_mul_f32_e32 v116, v156, v119
	v_cvt_pk_f16_f32 v82, v82, v83
	v_mul_f32_e32 v83, v156, v102
	v_mul_f32_e32 v84, v156, v103
	v_cvt_pk_f16_f32 v66, v66, v67
	v_mul_f32_e32 v67, v156, v70
	v_mul_f32_e32 v68, v156, v71
	v_cvt_pk_f16_f32 v50, v50, v51
	v_mul_f32_e32 v51, v156, v54
	v_mul_f32_e32 v52, v156, v55
	v_cvt_pk_f16_f32 v34, v34, v35
	v_mul_f32_e32 v35, v156, v38
	v_mul_f32_e32 v36, v156, v39
	v_cvt_pk_f16_f32 v18, v18, v19
	v_mul_f32_e32 v19, v156, v22
	v_mul_f32_e32 v20, v156, v23
	v_cvt_pk_f16_f32 v2, v2, v3
	v_mul_f32_e32 v3, v156, v6
	v_mul_f32_e32 v4, v156, v7
	v_cvt_pk_f16_f32 v115, v115, v116
	v_cvt_pk_f16_f32 v83, v83, v84
	v_cvt_pk_f16_f32 v67, v67, v68
	v_cvt_pk_f16_f32 v51, v51, v52
	v_cvt_pk_f16_f32 v35, v35, v36
	v_cvt_pk_f16_f32 v19, v19, v20
	v_cvt_pk_f16_f32 v3, v3, v4
	v_permlane32_swap_b32_e32 v112, v114
	v_permlane32_swap_b32_e32 v113, v115
	v_permlane32_swap_b32_e32 v80, v82
	v_permlane32_swap_b32_e32 v81, v83
	v_permlane32_swap_b32_e32 v64, v66
	v_permlane32_swap_b32_e32 v65, v67
	v_permlane32_swap_b32_e32 v48, v50
	v_permlane32_swap_b32_e32 v49, v51
	v_permlane32_swap_b32_e32 v32, v34
	v_permlane32_swap_b32_e32 v33, v35
	v_permlane32_swap_b32_e32 v16, v18
	v_permlane32_swap_b32_e32 v17, v19
	v_permlane32_swap_b32_e32 v0, v2
	v_permlane32_swap_b32_e32 v1, v3
	global_store_dwordx4 v157, v[112:115], s[4:5]
	global_store_dwordx4 v157, v[80:83], s[4:5] offset:128
	global_store_dwordx4 v157, v[64:67], s[4:5] offset:192
	v_mul_f32_e32 v112, v156, v120
	v_mul_f32_e32 v113, v156, v121
	v_mul_f32_e32 v80, v156, v104
	v_mul_f32_e32 v81, v156, v105
	v_mul_f32_e32 v64, v156, v72
	v_mul_f32_e32 v65, v156, v73
	global_store_dwordx4 v157, v[48:51], s[4:5] offset:256
	global_store_dwordx4 v157, v[32:35], s[4:5] offset:320
	global_store_dwordx4 v157, v[16:19], s[4:5] offset:384
	v_mul_f32_e32 v48, v156, v56
	v_mul_f32_e32 v49, v156, v57
	v_mul_f32_e32 v32, v156, v40
	v_mul_f32_e32 v33, v156, v41
	v_mul_f32_e32 v16, v156, v24
	v_mul_f32_e32 v17, v156, v25
	global_store_dwordx4 v157, v[0:3], s[4:5] offset:448
	v_cvt_pk_f16_f32 v112, v112, v113
	v_mul_f32_e32 v113, v156, v122
	v_mul_f32_e32 v0, v156, v8
	v_mul_f32_e32 v1, v156, v9
	v_mul_f32_e32 v114, v156, v123
	v_cvt_pk_f16_f32 v80, v80, v81
	v_mul_f32_e32 v81, v156, v106
	v_mul_f32_e32 v82, v156, v107
	v_cvt_pk_f16_f32 v64, v64, v65
	v_mul_f32_e32 v65, v156, v74
	v_mul_f32_e32 v66, v156, v75
	v_cvt_pk_f16_f32 v48, v48, v49
	v_mul_f32_e32 v49, v156, v58
	v_mul_f32_e32 v50, v156, v59
	v_cvt_pk_f16_f32 v32, v32, v33
	v_mul_f32_e32 v33, v156, v42
	v_mul_f32_e32 v34, v156, v43
	v_cvt_pk_f16_f32 v16, v16, v17
	v_mul_f32_e32 v17, v156, v26
	v_mul_f32_e32 v18, v156, v27
	v_cvt_pk_f16_f32 v0, v0, v1
	v_mul_f32_e32 v1, v156, v10
	v_mul_f32_e32 v2, v156, v11
	v_cvt_pk_f16_f32 v113, v113, v114
	v_mul_f32_e32 v114, v156, v124
	v_mul_f32_e32 v115, v156, v125
	v_cvt_pk_f16_f32 v81, v81, v82
	v_mul_f32_e32 v82, v156, v108
	v_mul_f32_e32 v83, v156, v109
	v_cvt_pk_f16_f32 v65, v65, v66
	v_mul_f32_e32 v66, v156, v76
	v_mul_f32_e32 v67, v156, v77
	v_cvt_pk_f16_f32 v49, v49, v50
	v_mul_f32_e32 v50, v156, v60
	v_mul_f32_e32 v51, v156, v61
	v_cvt_pk_f16_f32 v33, v33, v34
	v_mul_f32_e32 v34, v156, v44
	v_mul_f32_e32 v35, v156, v45
	v_cvt_pk_f16_f32 v17, v17, v18
	v_mul_f32_e32 v18, v156, v28
	v_mul_f32_e32 v19, v156, v29
	v_cvt_pk_f16_f32 v1, v1, v2
	v_mul_f32_e32 v2, v156, v12
	v_mul_f32_e32 v3, v156, v13
	v_cvt_pk_f16_f32 v114, v114, v115
	v_mul_f32_e32 v115, v156, v126
	v_mul_f32_e32 v116, v156, v127
	v_cvt_pk_f16_f32 v82, v82, v83
	v_mul_f32_e32 v83, v156, v110
	v_mul_f32_e32 v84, v156, v111
	v_cvt_pk_f16_f32 v66, v66, v67
	v_mul_f32_e32 v67, v156, v78
	v_mul_f32_e32 v68, v156, v79
	v_cvt_pk_f16_f32 v50, v50, v51
	v_mul_f32_e32 v51, v156, v62
	v_mul_f32_e32 v52, v156, v63
	v_cvt_pk_f16_f32 v34, v34, v35
	v_mul_f32_e32 v35, v156, v46
	v_mul_f32_e32 v36, v156, v47
	v_cvt_pk_f16_f32 v18, v18, v19
	v_mul_f32_e32 v19, v156, v30
	v_mul_f32_e32 v20, v156, v31
	v_cvt_pk_f16_f32 v2, v2, v3
	v_mul_f32_e32 v3, v156, v14
	v_mul_f32_e32 v4, v156, v15
	v_cvt_pk_f16_f32 v115, v115, v116
	v_cvt_pk_f16_f32 v83, v83, v84
	v_cvt_pk_f16_f32 v67, v67, v68
	v_cvt_pk_f16_f32 v51, v51, v52
	v_cvt_pk_f16_f32 v35, v35, v36
	v_cvt_pk_f16_f32 v19, v19, v20
	v_cvt_pk_f16_f32 v3, v3, v4
	v_permlane32_swap_b32_e32 v112, v114
	v_permlane32_swap_b32_e32 v113, v115
	v_permlane32_swap_b32_e32 v80, v82
	v_permlane32_swap_b32_e32 v81, v83
	v_permlane32_swap_b32_e32 v64, v66
	v_permlane32_swap_b32_e32 v65, v67
	v_permlane32_swap_b32_e32 v48, v50
	v_permlane32_swap_b32_e32 v49, v51
	v_permlane32_swap_b32_e32 v32, v34
	v_permlane32_swap_b32_e32 v33, v35
	v_permlane32_swap_b32_e32 v16, v18
	v_permlane32_swap_b32_e32 v17, v19
	v_permlane32_swap_b32_e32 v0, v2
	v_permlane32_swap_b32_e32 v1, v3
	s_add_i32 s94, s6, 2
	global_store_dwordx4 v157, v[112:115], s[4:5] offset:32
	global_store_dwordx4 v157, v[80:83], s[4:5] offset:160
	global_store_dwordx4 v157, v[64:67], s[4:5] offset:224
	global_store_dwordx4 v157, v[48:51], s[4:5] offset:288
	global_store_dwordx4 v157, v[32:35], s[4:5] offset:352
	global_store_dwordx4 v157, v[16:19], s[4:5] offset:416
	global_store_dwordx4 v157, v[0:3], s[4:5] offset:480
	s_mov_b64 s[4:5], exec
	v_readlane_b32 s2, v255, 49
	v_readlane_b32 s3, v255, 50
	s_and_b64 s[2:3], s[4:5], s[2:3]
	s_mov_b64 exec, s[2:3]
	s_cbranch_execz .LBB0_586
	s_or_b32 s2, s6, 1
	v_readlane_b32 s3, v255, 20
	s_cmp_lt_u32 s94, s3
	s_cselect_b32 s8, s94, s2
	s_lshr_b32 s2, s8, 2
	v_readlane_b32 s3, v255, 19
	s_mul_i32 s2, s2, s3
	v_readlane_b32 s3, v255, 18
	s_add_i32 s9, s2, s3
	s_lshl_b32 s2, s9, 6
	s_and_b32 s10, s2, 0xfffff000
	s_mul_i32 s6, s10, 0x6800
	v_readlane_b32 s15, v255, 21
	s_mul_hi_i32 s3, s10, 0x6800
	s_add_u32 s6, s15, s6
	v_readlane_b32 s16, v255, 22
	s_addc_u32 s3, s16, s3
	s_and_b32 s11, s2, 0xe00
	s_add_u32 s6, s6, s11
	s_addc_u32 s7, s3, 0
	s_add_u32 s2, s6, 0x3800
	s_addc_u32 s3, s7, 0
	s_lshl_b32 s12, s8, 8
	s_and_b32 s12, s12, 0x100
	s_add_u32 s6, s6, s12
	s_addc_u32 s7, s7, 0
	s_add_u32 s6, s6, 0x2800
	s_addc_u32 s7, s7, 0
	s_lshl_b32 s9, s9, 8
	s_and_b32 s9, s9, 0x700
	s_and_b32 s8, s8, 2
	s_xor_b32 s13, s9, 0xf00
	s_cmp_eq_u32 s8, 0
	s_cselect_b32 s8, s13, s9
	s_or_b32 s8, s8, s10
	s_mul_hi_i32 s9, s8, 0x6800
	s_mulk_i32 s8, 0x6800
	s_add_u32 s8, s15, s8
	s_addc_u32 s9, s16, s9
	s_add_u32 s8, s8, s11
	s_addc_u32 s9, s9, 0
	s_add_u32 s8, s8, s12
	s_addc_u32 s9, s9, 0
	s_add_u32 s8, s8, 0x1800
	v_readlane_b32 s10, v255, 46
	s_addc_u32 s9, s9, 0
	v_readlane_b32 s11, v255, 47
	v_mov_b64_e32 v[2:3], s[8:9]
	s_nop 0
	v_mov_b64_e32 v[0:1], s[10:11]
	ds_write_b64 v0, v[2:3]
	s_waitcnt lgkmcnt(0)
	v_mov_b64_e32 v[0:1], s[80:81]
	v_mov_b64_e32 v[2:3], s[6:7]
	ds_write_b64 v0, v[2:3]
	s_waitcnt lgkmcnt(0)
	v_mov_b64_e32 v[0:1], s[0:1]
	v_mov_b64_e32 v[2:3], s[2:3]
	ds_write_b64 v0, v[2:3]
	s_waitcnt lgkmcnt(0)
.LBB0_586:
	s_or_b64 exec, exec, s[4:5]
	v_mov_b32_e32 v38, v165
	v_readlane_b32 s5, v255, 51
	v_readfirstlane_b32 s2, v38
	s_ashr_i32 s79, s2, 6
	v_bfe_u32 v0, v38, 5, 1
	v_and_b32_e32 v176, 31, v38
	s_lshl_b32 s92, s79, 5
	v_lshlrev_b32_e32 v32, 2, v0
	s_add_i32 s74, s92, s74
	v_sub_u32_e32 v1, v176, v32
	v_lshlrev_b32_e32 v175, 4, v0
	s_lshl_b32 s2, s79, 3
	v_bfe_u32 v0, v38, 4, 2
	v_add_u32_e32 v179, s74, v1
	v_or_b32_e32 v1, s2, v0
	v_and_b32_e32 v2, 15, v38
	v_and_b32_e32 v39, 63, v38
	v_bitop3_b32 v3, v0, v38, 15 bitop3:0x78
	v_mul_lo_u32 v1, v1, s14
	v_bitop3_b32 v0, v0, v2, 4 bitop3:0x36
	s_mul_i32 s4, s79, 0x1c00
	s_waitcnt vmcnt(16)
	v_lshlrev_b32_e32 v40, 4, v39
	v_lshl_or_b32 v0, v0, 4, v1
	s_lshl_b32 s78, s79, 11
	v_readlane_b32 s7, v255, 53
	s_lshl_b32 s3, s79, 12
	s_add_i32 s4, s5, s4
	v_lshl_or_b32 v160, v3, 4, v1
	v_add_u32_e32 v170, 0x1a000, v0
	s_add_i32 s78, s78, s7
	s_add_i32 s3, s3, s33
	v_add_u32_e32 v180, s4, v40
	s_waitcnt vmcnt(16) lgkmcnt(0)
	ds_write_b128 v180, v[128:131]
	ds_write_b128 v180, v[132:135] offset:1024
	ds_write_b128 v180, v[136:139] offset:2048
	ds_write_b128 v180, v[140:143] offset:3072
	ds_write_b128 v180, v[144:147] offset:4096
	ds_write_b128 v180, v[148:151] offset:5120
	ds_write_b128 v180, v[152:155] offset:6144
	s_add_u32 s4, s66, 0x1a2900
	s_addc_u32 s5, s67, 0
	v_lshl_add_u64 v[0:1], s[4:5], 0, v[160:161]
	s_add_i32 s82, s78, 0x4000
	s_mov_b32 s6, m0
	s_mov_b32 m0, s82
	s_nop 0
	global_load_lds_dwordx4 v[0:1], off
	s_mov_b32 m0, s6
	v_mov_b32_e32 v171, v161
	v_lshl_add_u64 v[0:1], s[4:5], 0, v[170:171]
	s_add_i32 s84, s78, 0x4400
	s_mov_b32 s4, m0
	s_mov_b32 m0, s84
	s_nop 0
	global_load_lds_dwordx4 v[0:1], off
	s_mov_b32 m0, s4
	s_waitcnt lgkmcnt(0)
	s_barrier
	v_lshlrev_b32_e32 v0, 4, v38
	s_movk_i32 s4, 0x70
	v_lshlrev_b32_e32 v33, 8, v176
	v_and_b32_e32 v1, 0x70, v0
	v_bitop3_b32 v34, v175, v0, s4 bitop3:0x78
	s_movk_i32 s4, 0x60
	v_add_u32_e32 v2, s7, v33
	v_bitop3_b32 v35, v175, v1, 32 bitop3:0x36
	v_bitop3_b32 v36, v175, v1, 64 bitop3:0x36
	v_bitop3_b32 v37, v175, v1, s4 bitop3:0x36
	v_add_u32_e32 v181, v34, v2
	v_add_u32_e32 v182, v35, v2
	v_add_u32_e32 v183, v36, v2
	v_add_u32_e32 v184, v37, v2
	ds_read_b128 v[0:3], v181 offset:0
	ds_read_b128 v[4:7], v181 offset:0x2000
	ds_read_b128 v[8:11], v180 offset:0
	ds_read_b128 v[42:45], v182 offset:0
	ds_read_b128 v[46:49], v182 offset:0x2000
	ds_read_b128 v[50:53], v180 offset:0x400
	s_waitcnt lgkmcnt(3)
	s_nop 0
	v_mfma_f32_32x32x16_bf16 v[16:31], v[0:3], v[8:11], 0
	v_mfma_f32_32x32x16_bf16 v[0:15], v[4:7], v[8:11], 0
	ds_read_b128 v[54:57], v183 offset:0
	ds_read_b128 v[58:61], v183 offset:0x2000
	ds_read_b128 v[62:65], v180 offset:0x800
	s_waitcnt lgkmcnt(3)
	v_mfma_f32_32x32x16_bf16 v[16:31], v[42:45], v[50:53], v[16:31]
	v_mfma_f32_32x32x16_bf16 v[0:15], v[46:49], v[50:53], v[0:15]
	ds_read_b128 v[42:45], v184 offset:0
	ds_read_b128 v[46:49], v184 offset:0x2000
	ds_read_b128 v[50:53], v180 offset:0xc00
	s_waitcnt lgkmcnt(3)
	v_mfma_f32_32x32x16_bf16 v[16:31], v[54:57], v[62:65], v[16:31]
	v_mfma_f32_32x32x16_bf16 v[0:15], v[58:61], v[62:65], v[0:15]
	ds_read_b128 v[54:57], v181 offset:0x80
	ds_read_b128 v[58:61], v181 offset:0x2080
	ds_read_b128 v[62:65], v180 offset:0x1000
	s_waitcnt lgkmcnt(3)
	v_mfma_f32_32x32x16_bf16 v[16:31], v[42:45], v[50:53], v[16:31]
	v_mfma_f32_32x32x16_bf16 v[0:15], v[46:49], v[50:53], v[0:15]
	ds_read_b128 v[42:45], v182 offset:0x80
	ds_read_b128 v[46:49], v182 offset:0x2080
	ds_read_b128 v[50:53], v180 offset:0x1400
	s_waitcnt lgkmcnt(3)
	v_mfma_f32_32x32x16_bf16 v[16:31], v[54:57], v[62:65], v[16:31]
	v_mfma_f32_32x32x16_bf16 v[0:15], v[58:61], v[62:65], v[0:15]
	ds_read_b128 v[54:57], v183 offset:0x80
	ds_read_b128 v[58:61], v183 offset:0x2080
	ds_read_b128 v[62:65], v180 offset:0x1800
	s_waitcnt lgkmcnt(3)
	v_mfma_f32_32x32x16_bf16 v[16:31], v[42:45], v[50:53], v[16:31]
	v_mfma_f32_32x32x16_bf16 v[0:15], v[46:49], v[50:53], v[0:15]
	ds_read_b128 v[42:45], v184 offset:0x80
	ds_read_b128 v[46:49], v184 offset:0x2080
	s_waitcnt lgkmcnt(2)
	v_mfma_f32_32x32x16_bf16 v[16:31], v[54:57], v[62:65], v[16:31]
	v_mfma_f32_32x32x16_bf16 v[0:15], v[58:61], v[62:65], v[0:15]
	s_waitcnt lgkmcnt(0)
	v_mfma_f32_32x32x16_bf16 v[16:31], v[42:45], v[166:169], v[16:31]
	v_mfma_f32_32x32x16_bf16 v[0:15], v[46:49], v[166:169], v[0:15]
	s_bitcmp0_b32 s100, 8
	s_cbranch_scc1 .Lstg_a17
	s_waitcnt vmcnt(0)
	s_waitcnt lgkmcnt(0)
	s_barrier
